# v76 + max |e|^2 precomputed in the scan phase (|e|^2 moved before the second scan barrier); phase 3 reads it instead of a DPP reduction
# baseline (speedup 1.0000x reference)
_Z7vq_mainPKfPKiS0_PfPhPdPi:
	s_load_dwordx4 s[4:7], s[0:1], 0x0
	s_load_dwordx2 s[22:23], s[0:1], 0x10
	s_load_dwordx2 s[20:21], s[0:1], 0x18
	s_load_dwordx4 s[12:15], s[0:1], 0x20
	s_load_dwordx2 s[10:11], s[0:1], 0x30
	s_and_b32 s3, s2, 7
	s_lshl_b32 s3, s3, 6
	s_lshr_b32 s16, s2, 3
	s_add_i32 s16, s16, s3
	s_lshr_b32 s18, s16, 5
	s_mov_b32 s19, 0
	s_and_b32 s28, s16, 31
	s_lshl_b32 s28, s28, 4
	s_add_i32 s29, s28, 1
	v_readfirstlane_b32 s17, v0
	v_and_b32_e32 v1, 63, v0
	v_lshlrev_b32_e32 v66, 4, v0
	s_lshr_b32 s17, s17, 6
	s_lshl_b32 s24, s17, 4
	s_lshl_b32 s30, s18, 15
	s_lshl_b32 s31, s18, 23
	v_add_u32_e32 v67, 0x1000, v66
	v_add_u32_e32 v68, 0x2000, v66
	v_add_u32_e32 v69, 0x3000, v66
	v_add_u32_e32 v70, 0x4000, v66
	v_add_u32_e32 v71, 0x5000, v66
	v_add_u32_e32 v72, 0x6000, v66
	v_add_u32_e32 v73, 0x7000, v66
	s_movk_i32 s9, 0x810
	s_mov_b32 s3, 0x8100
	s_mul_i32 s36, s29, 0x810
	v_mov_b32_e32 v141, s36
	v_sub_u32_e32 v141, 0, v141
	s_waitcnt lgkmcnt(0)
	s_add_u32 s34, s6, s30
	s_addc_u32 s35, s7, 0
	s_add_u32 s32, s4, s31
	s_addc_u32 s33, s5, 0
	global_load_dwordx4 v[74:77], v66, s[34:35]
	global_load_dwordx4 v[78:81], v67, s[34:35]
	global_load_dwordx4 v[82:85], v68, s[34:35]
	global_load_dwordx4 v[86:89], v69, s[34:35]
	global_load_dwordx4 v[90:93], v70, s[34:35]
	global_load_dwordx4 v[94:97], v71, s[34:35]
	global_load_dwordx4 v[98:101], v72, s[34:35]
	global_load_dwordx4 v[102:105], v73, s[34:35]
	v_and_b32_e32 v150, 15, v0
	v_or_b32_e32 v150, s24, v150
	v_and_b32_e32 v151, 48, v0
	v_lshl_or_b32 v150, v150, 10, v151
	global_load_dwordx4 v[62:65], v150, s[22:23] offset:0
	global_load_dwordx4 v[58:61], v150, s[22:23] offset:64
	global_load_dwordx4 v[54:57], v150, s[22:23] offset:128
	global_load_dwordx4 v[50:53], v150, s[22:23] offset:192
	global_load_dwordx4 v[46:49], v150, s[22:23] offset:256
	global_load_dwordx4 v[42:45], v150, s[22:23] offset:320
	global_load_dwordx4 v[38:41], v150, s[22:23] offset:384
	global_load_dwordx4 v[34:37], v150, s[22:23] offset:448
	global_load_dwordx4 v[30:33], v150, s[22:23] offset:512
	global_load_dwordx4 v[26:29], v150, s[22:23] offset:576
	global_load_dwordx4 v[22:25], v150, s[22:23] offset:640
	global_load_dwordx4 v[18:21], v150, s[22:23] offset:704
	global_load_dwordx4 v[14:17], v150, s[22:23] offset:768
	global_load_dwordx4 v[10:13], v150, s[22:23] offset:832
	global_load_dwordx4 v[6:9], v150, s[22:23] offset:896
	global_load_dwordx4 v[2:5], v150, s[22:23] offset:960
	v_and_b32_e32 v138, 15, v0
	v_lshlrev_b32_e32 v139, 2, v1
	v_bfe_u32 v140, v0, 4, 2
	v_mov_b32_e32 v142, 1
	v_mov_b32_e32 v143, 4
	v_mov_b32_e32 v144, 0x11100
	v_lshlrev_b32_e32 v145, 8, v0
	v_lshlrev_b32_e32 v148, 3, v0
	v_mov_b32_e32 v152, 0
	v_mov_b32_e32 v153, 0
	ds_write_b64 v148, v[152:153] offset:32768
	ds_write_b64 v148, v[152:153] offset:34832
	ds_write_b64 v148, v[152:153] offset:36896
	ds_write_b64 v148, v[152:153] offset:38960
	ds_write_b64 v148, v[152:153] offset:41024
	ds_write_b64 v148, v[152:153] offset:43088
	ds_write_b64 v148, v[152:153] offset:45152
	ds_write_b64 v148, v[152:153] offset:47216
	ds_write_b64 v148, v[152:153] offset:49280
	ds_write_b64 v148, v[152:153] offset:51344
	ds_write_b64 v148, v[152:153] offset:53408
	ds_write_b64 v148, v[152:153] offset:55472
	ds_write_b64 v148, v[152:153] offset:57536
	ds_write_b64 v148, v[152:153] offset:59600
	ds_write_b64 v148, v[152:153] offset:61664
	ds_write_b64 v148, v[152:153] offset:63728
	v_cmp_gt_u32_e32 vcc, 16, v0
	s_and_saveexec_b64 s[30:31], vcc
	v_mul_u32_u24_e32 v151, 0x810, v0
	ds_write_b64 v151, v[152:153] offset:34816
	v_mov_b32_e32 v150, 0x11540
	v_mov_b32_e32 v149, 8
	ds_write_b32 v150, v149
	s_mov_b64 exec, s[30:31]
	s_waitcnt lgkmcnt(0)
	s_barrier
	s_waitcnt vmcnt(16)
	v_mad_u32_u24 v74, v74, s9, v141
	v_mad_u32_u24 v75, v75, s9, v141
	v_mad_u32_u24 v76, v76, s9, v141
	v_mad_u32_u24 v77, v77, s9, v141
	v_mad_u32_u24 v78, v78, s9, v141
	v_mad_u32_u24 v79, v79, s9, v141
	v_mad_u32_u24 v80, v80, s9, v141
	v_mad_u32_u24 v81, v81, s9, v141
	v_mad_u32_u24 v82, v82, s9, v141
	v_mad_u32_u24 v83, v83, s9, v141
	v_mad_u32_u24 v84, v84, s9, v141
	v_mad_u32_u24 v85, v85, s9, v141
	v_mad_u32_u24 v86, v86, s9, v141
	v_mad_u32_u24 v87, v87, s9, v141
	v_mad_u32_u24 v88, v88, s9, v141
	v_mad_u32_u24 v89, v89, s9, v141
	v_mad_u32_u24 v90, v90, s9, v141
	v_mad_u32_u24 v91, v91, s9, v141
	v_mad_u32_u24 v92, v92, s9, v141
	v_mad_u32_u24 v93, v93, s9, v141
	v_mad_u32_u24 v94, v94, s9, v141
	v_mad_u32_u24 v95, v95, s9, v141
	v_mad_u32_u24 v96, v96, s9, v141
	v_mad_u32_u24 v97, v97, s9, v141
	v_mad_u32_u24 v98, v98, s9, v141
	v_mad_u32_u24 v99, v99, s9, v141
	v_mad_u32_u24 v100, v100, s9, v141
	v_mad_u32_u24 v101, v101, s9, v141
	v_mad_u32_u24 v102, v102, s9, v141
	v_mad_u32_u24 v103, v103, s9, v141
	v_mad_u32_u24 v104, v104, s9, v141
	v_mad_u32_u24 v105, v105, s9, v141
	v_cmp_gt_u32_e64 s[36:37], s3, v74
	v_cmp_gt_u32_e64 s[38:39], s3, v75
	v_cmp_gt_u32_e64 s[40:41], s3, v76
	v_cmp_gt_u32_e64 s[42:43], s3, v77
	v_cmp_gt_u32_e64 s[44:45], s3, v78
	v_cmp_gt_u32_e64 s[46:47], s3, v79
	v_cmp_gt_u32_e64 s[48:49], s3, v80
	v_cmp_gt_u32_e64 s[50:51], s3, v81
	v_cmp_gt_u32_e64 s[52:53], s3, v82
	v_cmp_gt_u32_e64 s[54:55], s3, v83
	v_cmp_gt_u32_e64 s[56:57], s3, v84
	v_cmp_gt_u32_e64 s[58:59], s3, v85
	v_cmp_gt_u32_e64 s[60:61], s3, v86
	v_cmp_gt_u32_e64 s[62:63], s3, v87
	v_cmp_gt_u32_e64 s[64:65], s3, v88
	v_cmp_gt_u32_e64 s[66:67], s3, v89
	v_cmp_gt_u32_e64 s[68:69], s3, v90
	v_cmp_gt_u32_e64 s[70:71], s3, v91
	v_cmp_gt_u32_e64 s[72:73], s3, v92
	v_cmp_gt_u32_e64 s[74:75], s3, v93
	v_cmp_gt_u32_e64 s[76:77], s3, v94
	v_cmp_gt_u32_e64 s[78:79], s3, v95
	v_cmp_gt_u32_e64 s[80:81], s3, v96
	v_cmp_gt_u32_e64 s[82:83], s3, v97
	v_cmp_gt_u32_e64 s[84:85], s3, v98
	v_cmp_gt_u32_e64 s[86:87], s3, v99
	v_cmp_gt_u32_e64 s[88:89], s3, v100
	v_cmp_gt_u32_e64 s[90:91], s3, v101
	v_cmp_gt_u32_e64 s[92:93], s3, v102
	v_cmp_gt_u32_e64 s[94:95], s3, v103
	v_cmp_gt_u32_e64 s[96:97], s3, v104
	v_cmp_gt_u32_e64 s[98:99], s3, v105
	s_mov_b64 exec, s[36:37]
	ds_add_u32 v74, v142 offset:34816
	s_mov_b64 exec, s[38:39]
	ds_add_u32 v75, v142 offset:34816
	s_mov_b64 exec, s[40:41]
	ds_add_u32 v76, v142 offset:34816
	s_mov_b64 exec, s[42:43]
	ds_add_u32 v77, v142 offset:34816
	s_mov_b64 exec, s[44:45]
	ds_add_u32 v78, v142 offset:34816
	s_mov_b64 exec, s[46:47]
	ds_add_u32 v79, v142 offset:34816
	s_mov_b64 exec, s[48:49]
	ds_add_u32 v80, v142 offset:34816
	s_mov_b64 exec, s[50:51]
	ds_add_u32 v81, v142 offset:34816
	s_mov_b64 exec, s[52:53]
	ds_add_u32 v82, v142 offset:34816
	s_mov_b64 exec, s[54:55]
	ds_add_u32 v83, v142 offset:34816
	s_mov_b64 exec, s[56:57]
	ds_add_u32 v84, v142 offset:34816
	s_mov_b64 exec, s[58:59]
	ds_add_u32 v85, v142 offset:34816
	s_mov_b64 exec, s[60:61]
	ds_add_u32 v86, v142 offset:34816
	s_mov_b64 exec, s[62:63]
	ds_add_u32 v87, v142 offset:34816
	s_mov_b64 exec, s[64:65]
	ds_add_u32 v88, v142 offset:34816
	s_mov_b64 exec, s[66:67]
	ds_add_u32 v89, v142 offset:34816
	s_mov_b64 exec, s[68:69]
	ds_add_u32 v90, v142 offset:34816
	s_mov_b64 exec, s[70:71]
	ds_add_u32 v91, v142 offset:34816
	s_mov_b64 exec, s[72:73]
	ds_add_u32 v92, v142 offset:34816
	s_mov_b64 exec, s[74:75]
	ds_add_u32 v93, v142 offset:34816
	s_mov_b64 exec, s[76:77]
	ds_add_u32 v94, v142 offset:34816
	s_mov_b64 exec, s[78:79]
	ds_add_u32 v95, v142 offset:34816
	s_mov_b64 exec, s[80:81]
	ds_add_u32 v96, v142 offset:34816
	s_mov_b64 exec, s[82:83]
	ds_add_u32 v97, v142 offset:34816
	s_mov_b64 exec, s[84:85]
	ds_add_u32 v98, v142 offset:34816
	s_mov_b64 exec, s[86:87]
	ds_add_u32 v99, v142 offset:34816
	s_mov_b64 exec, s[88:89]
	ds_add_u32 v100, v142 offset:34816
	s_mov_b64 exec, s[90:91]
	ds_add_u32 v101, v142 offset:34816
	s_mov_b64 exec, s[92:93]
	ds_add_u32 v102, v142 offset:34816
	s_mov_b64 exec, s[94:95]
	ds_add_u32 v103, v142 offset:34816
	s_mov_b64 exec, s[96:97]
	ds_add_u32 v104, v142 offset:34816
	s_mov_b64 exec, s[98:99]
	ds_add_u32 v105, v142 offset:34816
	s_mov_b64 exec, -1
	s_waitcnt lgkmcnt(0)
	s_barrier
	s_waitcnt vmcnt(0)
	v_mul_f32_e32 v150, v62, v62
	v_mul_f32_e32 v151, v63, v63
	v_mul_f32_e32 v152, v64, v64
	v_mul_f32_e32 v153, v65, v65
	v_fmac_f32_e32 v150, v58, v58
	v_fmac_f32_e32 v151, v59, v59
	v_fmac_f32_e32 v152, v60, v60
	v_fmac_f32_e32 v153, v61, v61
	v_fmac_f32_e32 v150, v54, v54
	v_fmac_f32_e32 v151, v55, v55
	v_fmac_f32_e32 v152, v56, v56
	v_fmac_f32_e32 v153, v57, v57
	v_fmac_f32_e32 v150, v50, v50
	v_fmac_f32_e32 v151, v51, v51
	v_fmac_f32_e32 v152, v52, v52
	v_fmac_f32_e32 v153, v53, v53
	v_fmac_f32_e32 v150, v46, v46
	v_fmac_f32_e32 v151, v47, v47
	v_fmac_f32_e32 v152, v48, v48
	v_fmac_f32_e32 v153, v49, v49
	v_fmac_f32_e32 v150, v42, v42
	v_fmac_f32_e32 v151, v43, v43
	v_fmac_f32_e32 v152, v44, v44
	v_fmac_f32_e32 v153, v45, v45
	v_fmac_f32_e32 v150, v38, v38
	v_fmac_f32_e32 v151, v39, v39
	v_fmac_f32_e32 v152, v40, v40
	v_fmac_f32_e32 v153, v41, v41
	v_fmac_f32_e32 v150, v34, v34
	v_fmac_f32_e32 v151, v35, v35
	v_fmac_f32_e32 v152, v36, v36
	v_fmac_f32_e32 v153, v37, v37
	v_fmac_f32_e32 v150, v30, v30
	v_fmac_f32_e32 v151, v31, v31
	v_fmac_f32_e32 v152, v32, v32
	v_fmac_f32_e32 v153, v33, v33
	v_fmac_f32_e32 v150, v26, v26
	v_fmac_f32_e32 v151, v27, v27
	v_fmac_f32_e32 v152, v28, v28
	v_fmac_f32_e32 v153, v29, v29
	v_fmac_f32_e32 v150, v22, v22
	v_fmac_f32_e32 v151, v23, v23
	v_fmac_f32_e32 v152, v24, v24
	v_fmac_f32_e32 v153, v25, v25
	v_fmac_f32_e32 v150, v18, v18
	v_fmac_f32_e32 v151, v19, v19
	v_fmac_f32_e32 v152, v20, v20
	v_fmac_f32_e32 v153, v21, v21
	v_fmac_f32_e32 v150, v14, v14
	v_fmac_f32_e32 v151, v15, v15
	v_fmac_f32_e32 v152, v16, v16
	v_fmac_f32_e32 v153, v17, v17
	v_fmac_f32_e32 v150, v10, v10
	v_fmac_f32_e32 v151, v11, v11
	v_fmac_f32_e32 v152, v12, v12
	v_fmac_f32_e32 v153, v13, v13
	v_fmac_f32_e32 v150, v6, v6
	v_fmac_f32_e32 v151, v7, v7
	v_fmac_f32_e32 v152, v8, v8
	v_fmac_f32_e32 v153, v9, v9
	v_fmac_f32_e32 v150, v2, v2
	v_fmac_f32_e32 v151, v3, v3
	v_fmac_f32_e32 v152, v4, v4
	v_fmac_f32_e32 v153, v5, v5
	v_add_f32_e32 v150, v150, v151
	v_add_f32_e32 v152, v152, v153
	v_add_f32_e32 v150, v150, v152
	v_mbcnt_lo_u32_b32 v151, -1, 0
	v_mbcnt_hi_u32_b32 v151, -1, v151
	v_xor_b32_e32 v152, 16, v151
	v_lshlrev_b32_e32 v152, 2, v152
	ds_bpermute_b32 v152, v152, v150
	v_xor_b32_e32 v153, 32, v151
	v_lshlrev_b32_e32 v153, 2, v153
	s_waitcnt lgkmcnt(0)
	v_add_f32_e32 v150, v150, v152
	ds_bpermute_b32 v153, v153, v150
	v_add_u32_e32 v152, s24, v1
	v_lshlrev_b32_e32 v152, 2, v152
	v_add_u32_e32 v152, 0x11300, v152
	v_cmp_gt_u32_e32 vcc, 16, v1
	s_and_saveexec_b64 s[30:31], vcc
	s_waitcnt lgkmcnt(0)
	v_add_f32_e32 v150, v150, v153
	ds_write_b32 v152, v150
	s_mov_b64 exec, s[30:31]
	v_and_b32_e32 v67, 15, v0
	v_mul_u32_u24_e32 v67, 0x810, v67
	ds_read_b32 v68, v67 offset:34816
	s_waitcnt lgkmcnt(0)
	v_mov_b32_e32 v69, v68
	s_nop 1
	v_add_u32_dpp v69, v69, v69 row_shr:1 row_mask:0xf bank_mask:0xf bound_ctrl:1
	s_nop 1
	v_add_u32_dpp v69, v69, v69 row_shr:2 row_mask:0xf bank_mask:0xf bound_ctrl:1
	s_nop 1
	v_add_u32_dpp v69, v69, v69 row_shr:4 row_mask:0xf bank_mask:0xf bound_ctrl:1
	s_nop 1
	v_add_u32_dpp v69, v69, v69 row_shr:8 row_mask:0xf bank_mask:0xf bound_ctrl:1
	s_nop 1
	v_sub_u32_e32 v70, v69, v68
	v_lshlrev_b32_e32 v70, 2, v70
	v_readlane_b32 s8, v69, 15
	s_cmp_lg_u32 s17, 0
	s_cbranch_scc1 .Lfront_nocursor
	v_cmp_gt_u32_e32 vcc, 16, v1
	s_and_saveexec_b64 s[30:31], vcc
	ds_write_b32 v67, v70 offset:34820
	v_lshl_add_u32 v71, v1, 2, v144
	ds_write_b32 v71, v68
	v_max_i32_e32 v150, 1, v68
	v_cvt_f32_u32_e32 v150, v150
	v_div_scale_f32 v151, s[100:101], v150, v150, 1.0
	v_rcp_f32_e32 v152, v151
	v_div_scale_f32 v153, vcc, 1.0, v150, 1.0
	v_fma_f32 v154, -v151, v152, 1.0
	v_fmac_f32_e32 v152, v154, v152
	v_mul_f32_e32 v154, v153, v152
	v_fma_f32 v155, -v151, v154, v153
	v_fmac_f32_e32 v154, v155, v152
	v_fma_f32 v153, -v151, v154, v153
	v_div_fmas_f32 v155, v153, v152, v154
	v_div_fixup_f32 v156, v155, v150, 1.0
	ds_write_b32 v71, v156 offset:320
	s_mov_b64 exec, s[30:31]
.Lfront_nocursor:
	s_waitcnt lgkmcnt(0)
	s_barrier
	s_cmp_lg_u32 s17, 0
	s_cbranch_scc1 .Lfront_noe2m
	v_mov_b32_e32 v150, 0x11300
	v_lshl_or_b32 v150, v1, 2, v150
	ds_read_b32 v150, v150
	s_waitcnt lgkmcnt(0)
	s_nop 1
	v_mov_b32_dpp v151, v150 quad_perm:[1,0,3,2] row_mask:0xf bank_mask:0xf bound_ctrl:1
	v_max_f32_e32 v150, v150, v151
	s_nop 1
	v_mov_b32_dpp v151, v150 quad_perm:[2,3,0,1] row_mask:0xf bank_mask:0xf bound_ctrl:1
	v_max_f32_e32 v150, v150, v151
	s_nop 1
	v_mov_b32_dpp v151, v150 row_half_mirror row_mask:0xf bank_mask:0xf bound_ctrl:1
	v_max_f32_e32 v150, v150, v151
	s_nop 1
	v_mov_b32_dpp v151, v150 row_mirror row_mask:0xf bank_mask:0xf bound_ctrl:1
	v_max_f32_e32 v150, v150, v151
	s_nop 1
	v_readlane_b32 s100, v150, 0
	v_readlane_b32 s101, v150, 16
	v_readlane_b32 s30, v150, 32
	v_readlane_b32 s31, v150, 48
	s_nop 1
	v_mov_b32_e32 v151, s101
	v_max_f32_e32 v151, s100, v151
	v_mov_b32_e32 v152, s31
	v_max_f32_e32 v152, s30, v152
	v_max_f32_e32 v151, v151, v152
	v_mov_b32_e32 v152, 0x11280
	ds_write_b32 v152, v151
.Lfront_noe2m:
	s_mov_b64 exec, s[36:37]
	ds_add_rtn_u32 v106, v74, v143 offset:34820
	s_mov_b64 exec, s[38:39]
	ds_add_rtn_u32 v107, v75, v143 offset:34820
	s_mov_b64 exec, s[40:41]
	ds_add_rtn_u32 v108, v76, v143 offset:34820
	s_mov_b64 exec, s[42:43]
	ds_add_rtn_u32 v109, v77, v143 offset:34820
	s_mov_b64 exec, s[44:45]
	ds_add_rtn_u32 v110, v78, v143 offset:34820
	s_mov_b64 exec, s[46:47]
	ds_add_rtn_u32 v111, v79, v143 offset:34820
	s_mov_b64 exec, s[48:49]
	ds_add_rtn_u32 v112, v80, v143 offset:34820
	s_mov_b64 exec, s[50:51]
	ds_add_rtn_u32 v113, v81, v143 offset:34820
	s_mov_b64 exec, s[52:53]
	ds_add_rtn_u32 v114, v82, v143 offset:34820
	s_mov_b64 exec, s[54:55]
	ds_add_rtn_u32 v115, v83, v143 offset:34820
	s_mov_b64 exec, s[56:57]
	ds_add_rtn_u32 v116, v84, v143 offset:34820
	s_mov_b64 exec, s[58:59]
	ds_add_rtn_u32 v117, v85, v143 offset:34820
	s_mov_b64 exec, s[60:61]
	ds_add_rtn_u32 v118, v86, v143 offset:34820
	s_mov_b64 exec, s[62:63]
	ds_add_rtn_u32 v119, v87, v143 offset:34820
	s_mov_b64 exec, s[64:65]
	ds_add_rtn_u32 v120, v88, v143 offset:34820
	s_mov_b64 exec, s[66:67]
	ds_add_rtn_u32 v121, v89, v143 offset:34820
	s_mov_b64 exec, s[68:69]
	ds_add_rtn_u32 v122, v90, v143 offset:34820
	s_mov_b64 exec, s[70:71]
	ds_add_rtn_u32 v123, v91, v143 offset:34820
	s_mov_b64 exec, s[72:73]
	ds_add_rtn_u32 v124, v92, v143 offset:34820
	s_mov_b64 exec, s[74:75]
	ds_add_rtn_u32 v125, v93, v143 offset:34820
	s_mov_b64 exec, s[76:77]
	ds_add_rtn_u32 v126, v94, v143 offset:34820
	s_mov_b64 exec, s[78:79]
	ds_add_rtn_u32 v127, v95, v143 offset:34820
	s_mov_b64 exec, s[80:81]
	ds_add_rtn_u32 v128, v96, v143 offset:34820
	s_mov_b64 exec, s[82:83]
	ds_add_rtn_u32 v129, v97, v143 offset:34820
	s_mov_b64 exec, s[84:85]
	ds_add_rtn_u32 v130, v98, v143 offset:34820
	s_mov_b64 exec, s[86:87]
	ds_add_rtn_u32 v131, v99, v143 offset:34820
	s_mov_b64 exec, s[88:89]
	ds_add_rtn_u32 v132, v100, v143 offset:34820
	s_mov_b64 exec, s[90:91]
	ds_add_rtn_u32 v133, v101, v143 offset:34820
	s_mov_b64 exec, s[92:93]
	ds_add_rtn_u32 v134, v102, v143 offset:34820
	s_mov_b64 exec, s[94:95]
	ds_add_rtn_u32 v135, v103, v143 offset:34820
	s_mov_b64 exec, s[96:97]
	ds_add_rtn_u32 v136, v104, v143 offset:34820
	s_mov_b64 exec, s[98:99]
	ds_add_rtn_u32 v137, v105, v143 offset:34820
	s_mov_b64 exec, -1
	v_lshlrev_b32_e32 v145, 18, v0
	v_add_u32_e32 v146, 0x0, v145
	v_or_b32_e32 v74, v146, v74
	v_add_u32_e32 v147, 0x10000, v145
	v_or_b32_e32 v75, v147, v75
	v_add_u32_e32 v146, 0x20000, v145
	v_or_b32_e32 v76, v146, v76
	v_add_u32_e32 v147, 0x30000, v145
	v_or_b32_e32 v77, v147, v77
	v_add_u32_e32 v146, 0x4000000, v145
	v_or_b32_e32 v78, v146, v78
	v_add_u32_e32 v147, 0x4010000, v145
	v_or_b32_e32 v79, v147, v79
	v_add_u32_e32 v146, 0x4020000, v145
	v_or_b32_e32 v80, v146, v80
	v_add_u32_e32 v147, 0x4030000, v145
	v_or_b32_e32 v81, v147, v81
	v_add_u32_e32 v146, 0x8000000, v145
	v_or_b32_e32 v82, v146, v82
	v_add_u32_e32 v147, 0x8010000, v145
	v_or_b32_e32 v83, v147, v83
	v_add_u32_e32 v146, 0x8020000, v145
	v_or_b32_e32 v84, v146, v84
	v_add_u32_e32 v147, 0x8030000, v145
	v_or_b32_e32 v85, v147, v85
	v_add_u32_e32 v146, 0xc000000, v145
	v_or_b32_e32 v86, v146, v86
	v_add_u32_e32 v147, 0xc010000, v145
	v_or_b32_e32 v87, v147, v87
	v_add_u32_e32 v146, 0xc020000, v145
	v_or_b32_e32 v88, v146, v88
	v_add_u32_e32 v147, 0xc030000, v145
	v_or_b32_e32 v89, v147, v89
	v_add_u32_e32 v146, 0x10000000, v145
	v_or_b32_e32 v90, v146, v90
	v_add_u32_e32 v147, 0x10010000, v145
	v_or_b32_e32 v91, v147, v91
	v_add_u32_e32 v146, 0x10020000, v145
	v_or_b32_e32 v92, v146, v92
	v_add_u32_e32 v147, 0x10030000, v145
	v_or_b32_e32 v93, v147, v93
	v_add_u32_e32 v146, 0x14000000, v145
	v_or_b32_e32 v94, v146, v94
	v_add_u32_e32 v147, 0x14010000, v145
	v_or_b32_e32 v95, v147, v95
	v_add_u32_e32 v146, 0x14020000, v145
	v_or_b32_e32 v96, v146, v96
	v_add_u32_e32 v147, 0x14030000, v145
	v_or_b32_e32 v97, v147, v97
	v_add_u32_e32 v146, 0x18000000, v145
	v_or_b32_e32 v98, v146, v98
	v_add_u32_e32 v147, 0x18010000, v145
	v_or_b32_e32 v99, v147, v99
	v_add_u32_e32 v146, 0x18020000, v145
	v_or_b32_e32 v100, v146, v100
	v_add_u32_e32 v147, 0x18030000, v145
	v_or_b32_e32 v101, v147, v101
	v_add_u32_e32 v146, 0x1c000000, v145
	v_or_b32_e32 v102, v146, v102
	v_add_u32_e32 v147, 0x1c010000, v145
	v_or_b32_e32 v103, v147, v103
	v_add_u32_e32 v146, 0x1c020000, v145
	v_or_b32_e32 v104, v146, v104
	v_add_u32_e32 v147, 0x1c030000, v145
	v_or_b32_e32 v105, v147, v105
	s_waitcnt lgkmcnt(0)
	s_mov_b64 exec, s[36:37]
	ds_write_b32 v106, v74
	s_mov_b64 exec, s[38:39]
	ds_write_b32 v107, v75
	s_mov_b64 exec, s[40:41]
	ds_write_b32 v108, v76
	s_mov_b64 exec, s[42:43]
	ds_write_b32 v109, v77
	s_mov_b64 exec, s[44:45]
	ds_write_b32 v110, v78
	s_mov_b64 exec, s[46:47]
	ds_write_b32 v111, v79
	s_mov_b64 exec, s[48:49]
	ds_write_b32 v112, v80
	s_mov_b64 exec, s[50:51]
	ds_write_b32 v113, v81
	s_mov_b64 exec, s[52:53]
	ds_write_b32 v114, v82
	s_mov_b64 exec, s[54:55]
	ds_write_b32 v115, v83
	s_mov_b64 exec, s[56:57]
	ds_write_b32 v116, v84
	s_mov_b64 exec, s[58:59]
	ds_write_b32 v117, v85
	s_mov_b64 exec, s[60:61]
	ds_write_b32 v118, v86
	s_mov_b64 exec, s[62:63]
	ds_write_b32 v119, v87
	s_mov_b64 exec, s[64:65]
	ds_write_b32 v120, v88
	s_mov_b64 exec, s[66:67]
	ds_write_b32 v121, v89
	s_mov_b64 exec, s[68:69]
	ds_write_b32 v122, v90
	s_mov_b64 exec, s[70:71]
	ds_write_b32 v123, v91
	s_mov_b64 exec, s[72:73]
	ds_write_b32 v124, v92
	s_mov_b64 exec, s[74:75]
	ds_write_b32 v125, v93
	s_mov_b64 exec, s[76:77]
	ds_write_b32 v126, v94
	s_mov_b64 exec, s[78:79]
	ds_write_b32 v127, v95
	s_mov_b64 exec, s[80:81]
	ds_write_b32 v128, v96
	s_mov_b64 exec, s[82:83]
	ds_write_b32 v129, v97
	s_mov_b64 exec, s[84:85]
	ds_write_b32 v130, v98
	s_mov_b64 exec, s[86:87]
	ds_write_b32 v131, v99
	s_mov_b64 exec, s[88:89]
	ds_write_b32 v132, v100
	s_mov_b64 exec, s[90:91]
	ds_write_b32 v133, v101
	s_mov_b64 exec, s[92:93]
	ds_write_b32 v134, v102
	s_mov_b64 exec, s[94:95]
	ds_write_b32 v135, v103
	s_mov_b64 exec, s[96:97]
	ds_write_b32 v136, v104
	s_mov_b64 exec, s[98:99]
	ds_write_b32 v137, v105
	s_mov_b64 exec, -1
	s_waitcnt lgkmcnt(0)
	s_barrier
	v_or_b32_e32 v134, s24, v138
	v_lshlrev_b32_e32 v135, 3, v1
	v_lshlrev_b32_e32 v218, 4, v1
	v_lshlrev_b32_e32 v219, 3, v1
	v_mov_b32_e32 v223, 0x11540
	v_bfrev_b32_e32 v199, 1
	v_mov_b32_e32 v198, 1
	v_and_b32_e32 v221, 15, v1
	v_mov_b32_e32 v200, 0
	v_mov_b32_e32 v201, 0
	v_mov_b32_e32 v202, 0
	v_mov_b32_e32 v203, 0
	v_mov_b32_e32 v204, 0
	v_mov_b32_e32 v205, 0
	v_mov_b32_e32 v206, 0
	v_mov_b32_e32 v207, 0
	s_mov_b32 s50, -1
	s_branch .Lg0_start

.LBB0_118:
	s_waitcnt vmcnt(0)
	v_lshrrev_b32_e32 v67, 4, v0
	v_mov_b32_e32 v66, 0x11100
	v_lshl_or_b32 v66, v67, 2, v66
	s_waitcnt lgkmcnt(0)
	s_barrier
	ds_read_b32 v77, v66 offset:320
	v_mul_u32_u24_e32 v68, 0x102, v67
	v_lshlrev_b32_e32 v72, 3, v68
	v_lshl_add_u32 v68, v138, 3, v72
	v_add_u32_e32 v76, 0x8000, v68
	ds_read2_b64 v[68:71], v76 offset1:16
	v_mul_i32_i24_e32 v73, 0xfffffbf8, v67
	v_lshlrev_b32_e32 v66, 2, v138
	v_add3_u32 v78, v72, v73, v66
	ds_read2_b64 v[72:75], v76 offset0:32 offset1:48
	s_waitcnt lgkmcnt(1)
	v_cvt_f32_f64_e32 v68, v[68:69]
	v_cvt_f32_f64_e32 v69, v[70:71]
	v_mul_f32_e32 v68, v77, v68
	v_mul_f32_e32 v69, v77, v69
	v_fma_f32 v79, v68, v68, 0
	ds_write2_b32 v78, v68, v69 offset1:16
	s_waitcnt lgkmcnt(1)
	v_cvt_f32_f64_e32 v68, v[72:73]
	v_fmac_f32_e32 v79, v69, v69
	v_mul_f32_e32 v72, v77, v68
	ds_read2_b64 v[68:71], v76 offset0:64 offset1:80
	v_cvt_f32_f64_e32 v73, v[74:75]
	v_fmac_f32_e32 v79, v72, v72
	v_mul_f32_e32 v73, v77, v73
	v_fmac_f32_e32 v79, v73, v73
	ds_write2_b32 v78, v72, v73 offset0:32 offset1:48
	ds_read2_b64 v[72:75], v76 offset0:96 offset1:112
	s_waitcnt lgkmcnt(2)
	v_cvt_f32_f64_e32 v68, v[68:69]
	v_cvt_f32_f64_e32 v69, v[70:71]
	v_mul_f32_e32 v68, v77, v68
	v_mul_f32_e32 v69, v77, v69
	v_fmac_f32_e32 v79, v68, v68
	ds_write2_b32 v78, v68, v69 offset0:64 offset1:80
	s_waitcnt lgkmcnt(1)
	v_cvt_f32_f64_e32 v68, v[72:73]
	v_fmac_f32_e32 v79, v69, v69
	v_mul_f32_e32 v72, v77, v68
	ds_read2_b64 v[68:71], v76 offset0:128 offset1:144
	v_cvt_f32_f64_e32 v73, v[74:75]
	v_fmac_f32_e32 v79, v72, v72
	v_mul_f32_e32 v73, v77, v73
	v_fmac_f32_e32 v79, v73, v73
	ds_write2_b32 v78, v72, v73 offset0:96 offset1:112
	ds_read2_b64 v[72:75], v76 offset0:160 offset1:176
	s_waitcnt lgkmcnt(2)
	v_cvt_f32_f64_e32 v68, v[68:69]
	v_cvt_f32_f64_e32 v69, v[70:71]
	v_mul_f32_e32 v68, v77, v68
	v_mul_f32_e32 v69, v77, v69
	v_fmac_f32_e32 v79, v68, v68
	ds_write2_b32 v78, v68, v69 offset0:128 offset1:144
	s_waitcnt lgkmcnt(1)
	v_cvt_f32_f64_e32 v68, v[72:73]
	v_fmac_f32_e32 v79, v69, v69
	v_mul_f32_e32 v72, v77, v68
	ds_read2_b64 v[68:71], v76 offset0:192 offset1:208
	v_cvt_f32_f64_e32 v73, v[74:75]
	v_fmac_f32_e32 v79, v72, v72
	v_mul_f32_e32 v73, v77, v73
	v_fmac_f32_e32 v79, v73, v73
	ds_write2_b32 v78, v72, v73 offset0:160 offset1:176
	ds_read2_b64 v[72:75], v76 offset0:224 offset1:240
	s_waitcnt lgkmcnt(2)
	v_cvt_f32_f64_e32 v68, v[68:69]
	v_cvt_f32_f64_e32 v69, v[70:71]
	v_mul_f32_e32 v68, v77, v68
	v_mul_f32_e32 v69, v77, v69
	v_fmac_f32_e32 v79, v68, v68
	ds_write2_b32 v78, v68, v69 offset0:192 offset1:208
	s_waitcnt lgkmcnt(1)
	v_cvt_f32_f64_e32 v68, v[72:73]
	v_fmac_f32_e32 v79, v69, v69
	v_mul_f32_e32 v68, v77, v68
	v_cvt_f32_f64_e32 v69, v[74:75]
	v_fmac_f32_e32 v79, v68, v68
	v_mul_f32_e32 v69, v77, v69
	v_fmac_f32_e32 v79, v69, v69
	ds_write2_b32 v78, v68, v69 offset0:224 offset1:240
	v_cmp_eq_u32_e32 vcc, 0, v138
	v_add_f32_dpp v68, v79, v79 quad_perm:[1,0,3,2] row_mask:0xf bank_mask:0xf bound_ctrl:1
	s_nop 1
	v_add_f32_dpp v68, v68, v68 quad_perm:[2,3,0,1] row_mask:0xf bank_mask:0xf bound_ctrl:1
	s_nop 1
	v_add_f32_dpp v68, v68, v68 row_half_mirror row_mask:0xf bank_mask:0xf bound_ctrl:1
	s_nop 1
	v_mov_b32_dpp v69, v68 row_mirror row_mask:0xf bank_mask:0xf bound_ctrl:1
	s_and_saveexec_b64 s[0:1], vcc
	v_mov_b32_e32 v70, 0x11200
	v_lshl_or_b32 v67, v67, 2, v70
	v_add_f32_e32 v68, v68, v69
	ds_write_b32 v67, v68
	s_or_b64 exec, exec, s[0:1]
	v_lshlrev_b32_e32 v67, 2, v140
	s_movk_i32 s0, 0x408
	v_mad_u32_u24 v67, v138, s0, v67
	s_waitcnt lgkmcnt(0)
	s_barrier
	ds_read2_b32 v[68:69], v67 offset1:4
	ds_read2_b32 v[70:71], v67 offset0:64 offset1:68
	ds_read2_b32 v[72:73], v67 offset0:192 offset1:196
	s_lshl_b32 s29, s17, 2
	s_lshl_b32 s0, s24, 2
	s_waitcnt lgkmcnt(2)
	v_mfma_f32_16x16x4_f32 a[0:3], v68, v62, 0
	s_add_i32 s0, s0, 0x10100
	s_waitcnt lgkmcnt(1)
	v_mfma_f32_16x16x4_f32 a[4:7], v70, v63, 0
	ds_read2_b32 v[62:63], v67 offset0:128 offset1:132
	s_waitcnt lgkmcnt(0)
	v_mfma_f32_16x16x4_f32 a[0:3], v62, v64, a[0:3]
	v_mfma_f32_16x16x4_f32 a[4:7], v72, v65, a[4:7]
	v_mfma_f32_16x16x4_f32 a[0:3], v69, v58, a[0:3]
	v_mfma_f32_16x16x4_f32 a[4:7], v71, v59, a[4:7]
	ds_read2_b32 v[58:59], v67 offset0:8 offset1:12
	v_mfma_f32_16x16x4_f32 a[0:3], v63, v60, a[0:3]
	ds_read2_b32 v[62:63], v67 offset0:200 offset1:204
	v_mfma_f32_16x16x4_f32 a[4:7], v73, v61, a[4:7]
	ds_read2_b32 v[60:61], v67 offset0:72 offset1:76
	s_waitcnt lgkmcnt(2)
	v_mfma_f32_16x16x4_f32 a[0:3], v58, v54, a[0:3]
	s_waitcnt lgkmcnt(0)
	v_mfma_f32_16x16x4_f32 a[4:7], v60, v55, a[4:7]
	ds_read2_b32 v[54:55], v67 offset0:136 offset1:140
	s_waitcnt lgkmcnt(0)
	v_mfma_f32_16x16x4_f32 a[0:3], v54, v56, a[0:3]
	v_mfma_f32_16x16x4_f32 a[4:7], v62, v57, a[4:7]
	v_mfma_f32_16x16x4_f32 a[0:3], v59, v50, a[0:3]
	v_mfma_f32_16x16x4_f32 a[4:7], v61, v51, a[4:7]
	ds_read2_b32 v[50:51], v67 offset0:16 offset1:20
	v_mfma_f32_16x16x4_f32 a[0:3], v55, v52, a[0:3]
	ds_read2_b32 v[54:55], v67 offset0:208 offset1:212
	v_mfma_f32_16x16x4_f32 a[4:7], v63, v53, a[4:7]
	ds_read2_b32 v[52:53], v67 offset0:80 offset1:84
	s_waitcnt lgkmcnt(2)
	v_mfma_f32_16x16x4_f32 a[0:3], v50, v46, a[0:3]
	s_waitcnt lgkmcnt(0)
	v_mfma_f32_16x16x4_f32 a[4:7], v52, v47, a[4:7]
	ds_read2_b32 v[46:47], v67 offset0:144 offset1:148
	s_waitcnt lgkmcnt(0)
	v_mfma_f32_16x16x4_f32 a[0:3], v46, v48, a[0:3]
	v_mfma_f32_16x16x4_f32 a[4:7], v54, v49, a[4:7]
	v_mfma_f32_16x16x4_f32 a[0:3], v51, v42, a[0:3]
	v_mfma_f32_16x16x4_f32 a[4:7], v53, v43, a[4:7]
	ds_read2_b32 v[42:43], v67 offset0:24 offset1:28
	v_mfma_f32_16x16x4_f32 a[0:3], v47, v44, a[0:3]
	ds_read2_b32 v[46:47], v67 offset0:216 offset1:220
	v_mfma_f32_16x16x4_f32 a[4:7], v55, v45, a[4:7]
	ds_read2_b32 v[44:45], v67 offset0:88 offset1:92
	s_waitcnt lgkmcnt(2)
	v_mfma_f32_16x16x4_f32 a[0:3], v42, v38, a[0:3]
	s_waitcnt lgkmcnt(0)
	v_mfma_f32_16x16x4_f32 a[4:7], v44, v39, a[4:7]
	ds_read2_b32 v[38:39], v67 offset0:152 offset1:156
	s_waitcnt lgkmcnt(0)
	v_mfma_f32_16x16x4_f32 a[0:3], v38, v40, a[0:3]
	v_mfma_f32_16x16x4_f32 a[4:7], v46, v41, a[4:7]
	v_mfma_f32_16x16x4_f32 a[0:3], v43, v34, a[0:3]
	v_mfma_f32_16x16x4_f32 a[4:7], v45, v35, a[4:7]
	ds_read2_b32 v[34:35], v67 offset0:32 offset1:36
	v_mfma_f32_16x16x4_f32 a[0:3], v39, v36, a[0:3]
	ds_read2_b32 v[38:39], v67 offset0:224 offset1:228
	v_mfma_f32_16x16x4_f32 a[4:7], v47, v37, a[4:7]
	ds_read2_b32 v[36:37], v67 offset0:96 offset1:100
	s_waitcnt lgkmcnt(2)
	v_mfma_f32_16x16x4_f32 a[0:3], v34, v30, a[0:3]
	s_waitcnt lgkmcnt(0)
	v_mfma_f32_16x16x4_f32 a[4:7], v36, v31, a[4:7]
	ds_read2_b32 v[30:31], v67 offset0:160 offset1:164
	s_waitcnt lgkmcnt(0)
	v_mfma_f32_16x16x4_f32 a[0:3], v30, v32, a[0:3]
	v_mfma_f32_16x16x4_f32 a[4:7], v38, v33, a[4:7]
	v_mfma_f32_16x16x4_f32 a[0:3], v35, v26, a[0:3]
	v_mfma_f32_16x16x4_f32 a[4:7], v37, v27, a[4:7]
	ds_read2_b32 v[26:27], v67 offset0:40 offset1:44
	v_mfma_f32_16x16x4_f32 a[0:3], v31, v28, a[0:3]
	ds_read2_b32 v[30:31], v67 offset0:232 offset1:236
	v_mfma_f32_16x16x4_f32 a[4:7], v39, v29, a[4:7]
	ds_read2_b32 v[28:29], v67 offset0:104 offset1:108
	s_waitcnt lgkmcnt(2)
	v_mfma_f32_16x16x4_f32 a[0:3], v26, v22, a[0:3]
	s_waitcnt lgkmcnt(0)
	v_mfma_f32_16x16x4_f32 a[4:7], v28, v23, a[4:7]
	ds_read2_b32 v[22:23], v67 offset0:168 offset1:172
	s_waitcnt lgkmcnt(0)
	v_mfma_f32_16x16x4_f32 a[0:3], v22, v24, a[0:3]
	v_mfma_f32_16x16x4_f32 a[4:7], v30, v25, a[4:7]
	v_mfma_f32_16x16x4_f32 a[0:3], v27, v18, a[0:3]
	v_mfma_f32_16x16x4_f32 a[4:7], v29, v19, a[4:7]
	ds_read2_b32 v[18:19], v67 offset0:48 offset1:52
	v_mfma_f32_16x16x4_f32 a[0:3], v23, v20, a[0:3]
	ds_read2_b32 v[22:23], v67 offset0:240 offset1:244
	v_mfma_f32_16x16x4_f32 a[4:7], v31, v21, a[4:7]
	ds_read2_b32 v[20:21], v67 offset0:112 offset1:116
	s_waitcnt lgkmcnt(2)
	v_mfma_f32_16x16x4_f32 a[0:3], v18, v14, a[0:3]
	s_waitcnt lgkmcnt(0)
	v_mfma_f32_16x16x4_f32 a[4:7], v20, v15, a[4:7]
	ds_read2_b32 v[14:15], v67 offset0:176 offset1:180
	s_waitcnt lgkmcnt(0)
	v_mfma_f32_16x16x4_f32 a[0:3], v14, v16, a[0:3]
	v_mfma_f32_16x16x4_f32 a[4:7], v22, v17, a[4:7]
	v_mfma_f32_16x16x4_f32 a[0:3], v19, v10, a[0:3]
	v_mfma_f32_16x16x4_f32 a[4:7], v21, v11, a[4:7]
	ds_read2_b32 v[10:11], v67 offset0:56 offset1:60
	v_mfma_f32_16x16x4_f32 a[0:3], v15, v12, a[0:3]
	ds_read2_b32 v[14:15], v67 offset0:248 offset1:252
	v_mfma_f32_16x16x4_f32 a[4:7], v23, v13, a[4:7]
	ds_read2_b32 v[12:13], v67 offset0:120 offset1:124
	s_waitcnt lgkmcnt(2)
	v_mfma_f32_16x16x4_f32 a[0:3], v10, v6, a[0:3]
	s_waitcnt lgkmcnt(0)
	v_mfma_f32_16x16x4_f32 a[4:7], v12, v7, a[4:7]
	ds_read2_b32 v[6:7], v67 offset0:184 offset1:188
	s_waitcnt lgkmcnt(0)
	v_mfma_f32_16x16x4_f32 a[0:3], v6, v8, a[0:3]
	v_mfma_f32_16x16x4_f32 a[4:7], v14, v9, a[4:7]
	v_mfma_f32_16x16x4_f32 a[0:3], v11, v2, a[0:3]
	v_mov_b32_e32 v2, 0x11300
	v_lshl_add_u32 v2, v134, 2, v2
	ds_read_b32 v2, v2
	v_mfma_f32_16x16x4_f32 a[4:7], v13, v3, a[4:7]
	v_lshlrev_b32_e32 v3, 10, v140
	v_add3_u32 v3, s0, v66, v3
	v_mfma_f32_16x16x4_f32 a[0:3], v7, v4, a[0:3]
	v_or_b32_e32 v7, s29, v140
	v_lshl_or_b32 v4, v7, 8, v66
	v_add_u32_e32 v4, 0x10100, v4
	v_mfma_f32_16x16x4_f32 a[4:7], v15, v5, a[4:7]
	s_nop 9
	v_accvgpr_read_b32 v5, a0
	v_accvgpr_read_b32 v6, a1
	v_accvgpr_read_b32 v8, a2
	v_accvgpr_read_b32 v9, a3
	v_accvgpr_read_b32 v70, a4
	v_accvgpr_read_b32 v71, a5
	v_accvgpr_read_b32 v72, a6
	v_accvgpr_read_b32 v73, a7
	v_add_f32_e32 v5, v5, v70
	v_add_f32_e32 v6, v6, v71
	v_add_f32_e32 v8, v8, v72
	v_add_f32_e32 v9, v9, v73
	s_waitcnt lgkmcnt(0)
	v_fma_f32 v5, -2.0, v5, v2
	v_fma_f32 v6, -2.0, v6, v2
	v_fma_f32 v8, -2.0, v8, v2
	v_fmac_f32_e32 v2, -2.0, v9
	ds_write2st64_b32 v3, v5, v6 offset1:1
	ds_write2st64_b32 v3, v8, v2 offset0:2 offset1:3
	s_waitcnt lgkmcnt(0)
	s_barrier
	ds_read2_b32 v[2:3], v4 offset1:16
	ds_read2_b32 v[4:5], v4 offset0:32 offset1:48
	v_or_b32_e32 v6, 16, v138
	v_or_b32_e32 v8, 32, v138
	v_or_b32_e32 v9, 48, v138
	s_waitcnt lgkmcnt(1)
	v_cmp_lt_f32_e32 vcc, v3, v2
	s_nop 1
	v_cndmask_b32_e32 v10, v2, v3, vcc
	v_cndmask_b32_e32 v6, v138, v6, vcc
	s_waitcnt lgkmcnt(0)
	v_cmp_lt_f32_e32 vcc, v4, v10
	s_nop 1
	v_cndmask_b32_e32 v10, v10, v4, vcc
	v_cndmask_b32_e32 v8, v6, v8, vcc
	v_cmp_lt_f32_e32 vcc, v5, v10
	s_nop 1
	v_cndmask_b32_e32 v6, v10, v5, vcc
	v_cndmask_b32_e32 v14, v8, v9, vcc
	s_nop 0
	v_mov_b32_dpp v9, v6 quad_perm:[1,0,3,2] row_mask:0xf bank_mask:0xf bound_ctrl:1
	v_mov_b32_dpp v8, v14 quad_perm:[1,0,3,2] row_mask:0xf bank_mask:0xf bound_ctrl:1
	v_cmp_gt_f32_e64 s[4:5], v6, v9
	v_cmp_ngt_f32_e32 vcc, v6, v9
	s_and_saveexec_b64 s[6:7], vcc
	v_cmp_eq_f32_e32 vcc, v6, v9
	v_cmp_lt_i32_e64 s[0:1], v8, v14
	s_and_b64 s[0:1], vcc, s[0:1]
	s_andn2_b64 s[4:5], s[4:5], exec
	s_and_b64 s[0:1], s[0:1], exec
	s_or_b64 s[4:5], s[4:5], s[0:1]
	s_or_b64 exec, exec, s[6:7]
	s_and_saveexec_b64 s[0:1], s[4:5]
	v_mov_b32_e32 v6, v9
	v_mov_b32_e32 v14, v8
	s_or_b64 exec, exec, s[0:1]
	v_mov_b32_dpp v9, v6 quad_perm:[2,3,0,1] row_mask:0xf bank_mask:0xf bound_ctrl:1
	v_mov_b32_dpp v8, v14 quad_perm:[2,3,0,1] row_mask:0xf bank_mask:0xf bound_ctrl:1
	v_cmp_gt_f32_e64 s[4:5], v6, v9
	v_cmp_ngt_f32_e32 vcc, v6, v9
	s_and_saveexec_b64 s[6:7], vcc
	v_cmp_eq_f32_e32 vcc, v6, v9
	v_cmp_lt_i32_e64 s[0:1], v8, v14
	s_and_b64 s[0:1], vcc, s[0:1]
	s_andn2_b64 s[4:5], s[4:5], exec
	s_and_b64 s[0:1], s[0:1], exec
	s_or_b64 s[4:5], s[4:5], s[0:1]
	s_or_b64 exec, exec, s[6:7]
	s_and_saveexec_b64 s[0:1], s[4:5]
	v_mov_b32_e32 v6, v9
	v_mov_b32_e32 v14, v8
	s_or_b64 exec, exec, s[0:1]
	v_mov_b32_dpp v9, v6 row_half_mirror row_mask:0xf bank_mask:0xf bound_ctrl:1
	v_mov_b32_dpp v8, v14 row_half_mirror row_mask:0xf bank_mask:0xf bound_ctrl:1
	v_cmp_gt_f32_e64 s[4:5], v6, v9
	v_cmp_ngt_f32_e32 vcc, v6, v9
	s_and_saveexec_b64 s[6:7], vcc
	v_cmp_eq_f32_e32 vcc, v6, v9
	v_cmp_lt_i32_e64 s[0:1], v8, v14
	s_and_b64 s[0:1], vcc, s[0:1]
	s_andn2_b64 s[4:5], s[4:5], exec
	s_and_b64 s[0:1], s[0:1], exec
	s_or_b64 s[4:5], s[4:5], s[0:1]
	s_or_b64 exec, exec, s[6:7]
	s_and_saveexec_b64 s[0:1], s[4:5]
	v_mov_b32_e32 v6, v9
	v_mov_b32_e32 v14, v8
	s_or_b64 exec, exec, s[0:1]
	v_mov_b32_dpp v8, v6 row_mirror row_mask:0xf bank_mask:0xf bound_ctrl:1
	v_mov_b32_dpp v9, v14 row_mirror row_mask:0xf bank_mask:0xf bound_ctrl:1
	v_cmp_gt_f32_e64 s[4:5], v6, v8
	v_cmp_ngt_f32_e32 vcc, v6, v8
	s_and_saveexec_b64 s[6:7], vcc
	v_cmp_eq_f32_e32 vcc, v6, v8
	v_cmp_lt_i32_e64 s[0:1], v9, v14
	s_and_b64 s[0:1], vcc, s[0:1]
	s_andn2_b64 s[4:5], s[4:5], exec
	s_and_b64 s[0:1], s[0:1], exec
	s_or_b64 s[4:5], s[4:5], s[0:1]
	s_or_b64 exec, exec, s[6:7]
	s_and_saveexec_b64 s[0:1], s[4:5]
	v_mov_b32_e32 v6, v8
	v_mov_b32_e32 v14, v9
	s_or_b64 exec, exec, s[0:1]
	v_mov_b32_e32 v8, 0x11280
	ds_read_b32 v8, v8
	v_mov_b32_e32 v9, 0x11200
	v_lshl_add_u32 v7, v7, 2, v9
	ds_read_b32 v9, v7
	v_mov_b32_e32 v13, 0x260
	v_lshlrev_b32_e32 v18, 2, v139
	v_mov_b32_e32 v19, 0
	s_mov_b32 s25, 0
	s_mov_b32 s26, s25
	s_mov_b32 s0, 0x3f800347
	s_mov_b32 s1, 0x3f8020c5
	s_waitcnt lgkmcnt(0)
	v_pk_mul_f32 v[8:9], v[8:9], s[0:1]
	s_mov_b32 s4, 0xf800000
	v_mul_f32_e32 v7, 0x4f800000, v9
	v_cmp_gt_f32_e32 vcc, s4, v9
	s_nop 1
	v_cndmask_b32_e32 v7, v9, v7, vcc
	v_sqrt_f32_e32 v10, v7
	s_nop 0
	v_add_u32_e32 v11, -1, v10
	v_fma_f32 v12, -v11, v10, v7
	v_cmp_ge_f32_e64 s[0:1], 0, v12
	v_add_u32_e32 v12, 1, v10
	s_nop 0
	v_cndmask_b32_e64 v11, v10, v11, s[0:1]
	v_fma_f32 v10, -v12, v10, v7
	v_cmp_lt_f32_e64 s[0:1], 0, v10
	s_nop 1
	v_cndmask_b32_e64 v10, v11, v12, s[0:1]
	v_mul_f32_e32 v11, 0x37800000, v10
	v_cndmask_b32_e32 v10, v10, v11, vcc
	v_mul_f32_e32 v11, 0x4f800000, v8
	v_cmp_gt_f32_e32 vcc, s4, v8
	v_cmp_class_f32_e64 s[0:1], v7, v13
	s_nop 0
	v_cndmask_b32_e32 v11, v8, v11, vcc
	v_sqrt_f32_e32 v12, v11
	v_cndmask_b32_e64 v7, v10, v7, s[0:1]
	v_add_u32_e32 v10, -1, v12
	v_fma_f32 v15, -v10, v12, v11
	v_cmp_ge_f32_e64 s[0:1], 0, v15
	v_add_u32_e32 v15, 1, v12
	s_nop 0
	v_cndmask_b32_e64 v10, v12, v10, s[0:1]
	v_fma_f32 v12, -v15, v12, v11
	v_cmp_lt_f32_e64 s[0:1], 0, v12
	s_nop 1
	v_cndmask_b32_e64 v10, v10, v15, s[0:1]
	v_mul_f32_e32 v12, 0x37800000, v10
	v_cndmask_b32_e32 v10, v10, v12, vcc
	v_cmp_class_f32_e32 vcc, v11, v13
	s_mov_b32 s0, 0x380637bd
	s_mov_b32 s1, 0x350637bd
	v_cndmask_b32_e32 v10, v10, v11, vcc
	v_mul_f32_e32 v7, v7, v10
	v_mul_f32_e32 v7, 0x3f800347, v7
	v_pk_mul_f32 v[8:9], v[8:9], s[0:1]
	s_nop 0
	v_fmamk_f32 v7, v7, 0x3888509c, v9
	v_add_f32_e32 v7, v8, v7
	v_add_f32_e32 v7, 0xda24260, v7
	v_add_f32_e32 v6, v6, v7
	v_cmp_le_f32_e64 s[8:9], v2, v6
	v_cmp_le_f32_e64 s[6:7], v3, v6
	v_cmp_le_f32_e64 s[4:5], v4, v6
	v_lshl_add_u64 v[2:3], s[22:23], 0, v[18:19]
	s_and_b32 s19, s8, 0xffff
	s_lshl_b32 s22, s6, 16
	v_cmp_le_f32_e64 s[0:1], v5, v6
	s_or_b32 s24, s19, s22
	s_and_b32 s23, s4, 0xffff
	s_mov_b32 s22, s25
	s_or_b64 s[22:23], s[24:25], s[22:23]
	s_lshl_b32 s27, s0, 16
	s_or_b64 s[26:27], s[22:23], s[26:27]
	s_add_u32 s22, s26, -1
	s_addc_u32 s23, s27, -1
	s_and_b64 s[22:23], s[26:27], s[22:23]
	s_cmp_eq_u64 s[22:23], 0
	v_readlane_b32 s22, v14, 0
	s_cbranch_scc1 .LBB0_139
	s_lshl_b32 s19, s29, 2
	s_add_i32 s19, s19, 0x11100
	v_mov_b32_e32 v4, s19
	ds_read_b32 v4, v4
	s_mul_i32 s19, s17, 0x2040
	v_add_u32_e32 v8, s19, v135
	v_mov_b32_e32 v15, 0x7f800000
	s_waitcnt lgkmcnt(0)
	v_max_i32_e32 v4, 1, v4
	v_cvt_f64_u32_e32 v[12:13], v4
	v_div_scale_f64 v[16:17], s[30:31], v[12:13], v[12:13], 1.0
	v_rcp_f64_e32 v[20:21], v[16:17]
	v_div_scale_f64 v[22:23], vcc, 1.0, v[12:13], 1.0
	ds_read2st64_b64 v[4:7], v8 offset0:64 offset1:65
	ds_read2st64_b64 v[8:11], v8 offset0:66 offset1:67
	v_fma_f64 v[24:25], -v[16:17], v[20:21], 1.0
	v_fmac_f64_e32 v[20:21], v[20:21], v[24:25]
	v_fma_f64 v[24:25], -v[16:17], v[20:21], 1.0
	v_fmac_f64_e32 v[20:21], v[20:21], v[24:25]
	v_mul_f64 v[24:25], v[22:23], v[20:21]
	v_fma_f64 v[16:17], -v[16:17], v[24:25], v[22:23]
	v_div_fmas_f64 v[16:17], v[16:17], v[20:21], v[24:25]
	v_div_fixup_f64 v[12:13], v[16:17], v[12:13], 1.0
	s_waitcnt lgkmcnt(1)
	v_mul_f64 v[6:7], v[6:7], v[12:13]
	v_mul_f64 v[4:5], v[4:5], v[12:13]
	s_waitcnt lgkmcnt(0)
	v_mul_f64 v[8:9], v[8:9], v[12:13]
	v_mul_f64 v[10:11], v[12:13], v[10:11]
	v_mul_f64 v[12:13], v[6:7], v[6:7]
	v_fmac_f64_e32 v[12:13], v[4:5], v[4:5]
	v_fmac_f64_e32 v[12:13], v[8:9], v[8:9]
	v_fmac_f64_e32 v[12:13], v[10:11], v[10:11]
	s_nop 1
	v_mov_b32_dpp v16, v12 quad_perm:[1,0,3,2] row_mask:0xf bank_mask:0xf bound_ctrl:1
	v_mov_b32_dpp v17, v13 quad_perm:[1,0,3,2] row_mask:0xf bank_mask:0xf bound_ctrl:1
	v_add_f64 v[12:13], v[12:13], v[16:17]
	s_nop 1
	v_mov_b32_dpp v16, v12 quad_perm:[2,3,0,1] row_mask:0xf bank_mask:0xf bound_ctrl:1
	v_mov_b32_dpp v17, v13 quad_perm:[2,3,0,1] row_mask:0xf bank_mask:0xf bound_ctrl:1
	v_add_f64 v[12:13], v[12:13], v[16:17]
	s_nop 1
	v_mov_b32_dpp v16, v12 row_half_mirror row_mask:0xf bank_mask:0xf bound_ctrl:1
	v_mov_b32_dpp v17, v13 row_half_mirror row_mask:0xf bank_mask:0xf bound_ctrl:1
	v_add_f64 v[12:13], v[12:13], v[16:17]
	s_nop 1
	v_mov_b32_dpp v16, v12 row_mirror row_mask:0xf bank_mask:0xf bound_ctrl:1
	v_mov_b32_dpp v17, v13 row_mirror row_mask:0xf bank_mask:0xf bound_ctrl:1
	v_add_f64 v[12:13], v[12:13], v[16:17]
	s_nop 0
	v_readlane_b32 s19, v13, 16
	v_readlane_b32 s23, v12, 16
	v_readlane_b32 s31, v13, 0
	v_readlane_b32 s30, v12, 0
	v_mov_b32_e32 v16, s23
	v_mov_b32_e32 v17, s19
	v_readlane_b32 s19, v13, 48
	v_readlane_b32 s23, v12, 48
	v_add_f64 v[16:17], s[30:31], v[16:17]
	v_readlane_b32 s31, v13, 32
	v_readlane_b32 s30, v12, 32
	v_mov_b32_e32 v12, s23
	v_mov_b32_e32 v13, s19
	v_add_f64 v[12:13], s[30:31], v[12:13]
	v_add_f64 v[12:13], v[16:17], v[12:13]
